# P12 gather loop: x/norm loads of column chunks 1-3 hoisted to the top of each token iteration with counted vmcnt; P5->P6 grid barrier replaced by a workgroup-level sync (t1 is re-read tile for tile by
# speedup vs baseline: 1.0072x; 1.0002x over previous
.LBB0_1304:
	s_cmp_gt_i32 s95, 6
	s_cselect_b64 s[0:1], -1, 0
	s_and_b64 s[2:3], s[2:3], s[0:1]
	s_andn2_b64 vcc, exec, s[2:3]
	s_cbranch_vccnz .LBB0_1354
	s_waitcnt vmcnt(0)
	v_cmp_eq_u32_e32 vcc, 0, v0
	s_waitcnt vmcnt(0)
	s_barrier
	s_and_saveexec_b64 s[2:3], vcc
.LBB0_1353:
	s_or_b64 exec, exec, s[2:3]
	s_waitcnt lgkmcnt(0)
	s_barrier

.LBB0_2468:
	global_load_dwordx4 v[150:153], v5, s[16:17]
	global_load_dwordx4 v[154:157], v138, s[16:17]
	global_load_dwordx4 v[158:161], v139, s[16:17]
	global_load_dwordx4 v[162:165], v140, s[16:17]
	global_load_dwordx4 v[166:169], v141, s[16:17]
	global_load_dwordx4 v[170:173], v142, s[16:17]
	global_load_dwordx4 v[174:177], v143, s[16:17]
	global_load_dwordx4 v[178:181], v144, s[16:17]
	global_load_dwordx4 v[182:185], v[112:113], off offset:-3072
	global_load_dwordx4 v[186:189], v[40:41], off offset:16
	global_load_dwordx4 v[190:193], v[40:41], off
	global_load_dwordx4 v[198:201], v[112:113], off offset:-2048
	global_load_dwordx4 v[210:213], v[40:41], off offset:2048
	global_load_dwordx4 v[214:217], v[40:41], off offset:2064
	global_load_dwordx4 v[202:205], v[112:113], off offset:-1024
	global_load_dwordx4 v[218:221], v[42:43], off
	global_load_dwordx4 v[222:225], v[42:43], off offset:16
	global_load_dwordx4 v[206:209], v[112:113], off
	global_load_dwordx4 v[226:229], v[44:45], off
	global_load_dwordx4 v[230:233], v[44:45], off offset:16
	v_mov_b32_e32 v4, s11
	ds_read2_b32 v[114:115], v4 offset1:1
	ds_read2_b32 v[116:117], v4 offset0:2 offset1:3
	v_mov_b32_e32 v194, 0
	v_mov_b32_e32 v195, 0
	s_add_i32 s15, s15, 8
	s_waitcnt lgkmcnt(1)
	v_ashrrev_i32_e32 v119, 31, v114
	v_mov_b32_e32 v118, v114
	v_ashrrev_i32_e32 v121, 31, v115
	v_mov_b32_e32 v120, v115
	s_waitcnt lgkmcnt(0)
	v_ashrrev_i32_e32 v115, 31, v116
	v_mov_b32_e32 v114, v116
	v_ashrrev_i32_e32 v197, 31, v117
	v_mov_b32_e32 v196, v117
	v_lshlrev_b64 v[116:117], 11, v[120:121]
	v_lshlrev_b64 v[118:119], 11, v[118:119]
	v_lshlrev_b64 v[120:121], 11, v[196:197]
	v_lshlrev_b64 v[196:197], 11, v[114:115]
	v_lshl_add_u64 v[114:115], v[46:47], 0, v[118:119]
	v_lshl_add_u64 v[118:119], v[46:47], 0, v[196:197]
	v_lshl_add_u64 v[116:117], v[46:47], 0, v[116:117]
	v_lshl_add_u64 v[120:121], v[46:47], 0, v[120:121]
	s_addk_i32 s11, 0x80
	s_add_u32 s16, s16, 0x80
	s_addc_u32 s17, s17, 0
	s_cmp_gt_u32 s15, 55
	s_waitcnt vmcnt(19)
	v_mov_b32_e32 v196, v150
	s_waitcnt vmcnt(18)
	v_mov_b32_e32 v197, v154
	v_mov_b32_e32 v154, v151
	v_mov_b32_e32 v150, v152
	v_mov_b32_e32 v151, v156
	v_mov_b32_e32 v156, v153
	s_waitcnt vmcnt(17)
	v_mov_b32_e32 v152, v159
	v_mov_b32_e32 v153, v160
	v_mov_b32_e32 v159, v161
	v_pk_add_f32 v[154:155], v[196:197], v[154:155]
	v_pk_add_f32 v[150:151], v[150:151], v[156:157]
	v_pk_add_f32 v[152:153], v[152:153], v[158:159]
	v_pk_add_f32 v[150:151], v[154:155], v[150:151]
	v_pk_add_f32 v[152:153], v[152:153], v[152:153] op_sel:[0,1] op_sel_hi:[1,0]
	v_add_f32_e32 v4, 0, v150
	s_waitcnt vmcnt(16)
	v_add_f32_e32 v160, v162, v163
	v_add_f32_e32 v162, v164, v165
	s_waitcnt vmcnt(15)
	v_mov_b32_e32 v165, v166
	v_mov_b32_e32 v161, v168
	v_mov_b32_e32 v163, v169
	v_mov_b32_e32 v153, v167
	v_add_f32_e32 v164, v4, v151
	s_waitcnt vmcnt(14)
	v_mov_b32_e32 v168, v171
	v_mov_b32_e32 v169, v172
	v_mov_b32_e32 v171, v173
	v_pk_add_f32 v[156:157], v[160:161], v[162:163]
	v_pk_add_f32 v[150:151], v[164:165], v[152:153]
	v_pk_add_f32 v[158:159], v[168:169], v[170:171]
	v_pk_add_f32 v[150:151], v[150:151], v[156:157]
	v_pk_add_f32 v[154:155], v[158:159], v[158:159] op_sel:[0,1] op_sel_hi:[1,0]
	v_pk_add_f32 v[150:151], v[150:151], v[150:151] op_sel:[0,1] op_sel_hi:[1,0]
	s_waitcnt vmcnt(13)
	v_add_f32_e32 v172, v174, v175
	v_add_f32_e32 v174, v176, v177
	s_waitcnt vmcnt(12)
	v_mov_b32_e32 v173, v180
	v_mov_b32_e32 v175, v181
	v_mov_b32_e32 v155, v179
	v_mov_b32_e32 v151, v178
	v_pk_add_f32 v[160:161], v[172:173], v[174:175]
	v_pk_add_f32 v[150:151], v[150:151], v[154:155]
	s_waitcnt vmcnt(11)
	v_lshlrev_b32_e32 v176, 16, v182
	v_pk_add_f32 v[150:151], v[150:151], v[160:161]
	v_and_b32_e32 v177, 0xffff0000, v182
	v_add_f32_e32 v4, v150, v151
	v_fmamk_f32 v4, v4, 0x3a000000, v145
	v_rsq_f32_e32 v4, v4
	v_lshlrev_b32_e32 v180, 16, v183
	v_and_b32_e32 v181, 0xffff0000, v183
	v_lshlrev_b32_e32 v182, 16, v184
	v_and_b32_e32 v183, 0xffff0000, v184
	v_mul_f32_e32 v4, 0x41000000, v4
	v_pk_mul_f32 v[150:151], v[4:5], v[176:177] op_sel_hi:[0,1]
	v_pk_mul_f32 v[152:153], v[4:5], v[180:181] op_sel_hi:[0,1]
	v_pk_mul_f32 v[154:155], v[4:5], v[182:183] op_sel_hi:[0,1]
	s_waitcnt vmcnt(9)
	v_pk_mul_f32 v[152:153], v[192:193], v[152:153]
	v_pk_mul_f32 v[150:151], v[190:191], v[150:151]
	v_pk_mul_f32 v[154:155], v[186:187], v[154:155]
	v_med3_f32 v147, v150, s27, v146
	v_med3_f32 v150, v151, s27, v146
	v_med3_f32 v151, v152, s27, v146
	v_med3_f32 v152, v153, s27, v146
	v_med3_f32 v153, v154, s27, v146
	v_med3_f32 v154, v155, s27, v146
	v_lshlrev_b32_e32 v184, 16, v185
	v_and_b32_e32 v185, 0xffff0000, v185
	v_cvt_pk_fp8_f32 v194, v147, v150
	v_cvt_pk_fp8_f32 v195, v153, v154
	v_pk_mul_f32 v[156:157], v[4:5], v[184:185] op_sel_hi:[0,1]
	v_pk_mul_f32 v[156:157], v[188:189], v[156:157]
	v_cvt_pk_fp8_f32 v194, v151, v152 op_sel:[0,0,1]
	v_med3_f32 v155, v156, s27, v146
	v_med3_f32 v156, v157, s27, v146
	v_cvt_pk_fp8_f32 v195, v155, v156 op_sel:[0,0,1]
	global_store_dwordx2 v[114:115], v[194:195], off
	global_store_dwordx2 v[116:117], v[194:195], off
	global_store_dwordx2 v[118:119], v[194:195], off
	global_store_dwordx2 v[120:121], v[194:195], off
	v_mov_b32_e32 v162, 0
	v_mov_b32_e32 v163, 0
	s_waitcnt vmcnt(12)
	v_lshlrev_b32_e32 v164, 16, v198
	v_and_b32_e32 v165, 0xffff0000, v198
	v_lshlrev_b32_e32 v150, 16, v199
	v_and_b32_e32 v151, 0xffff0000, v199
	v_lshlrev_b32_e32 v166, 16, v200
	v_and_b32_e32 v167, 0xffff0000, v200
	v_pk_mul_f32 v[164:165], v[4:5], v[164:165] op_sel_hi:[0,1]
	v_pk_mul_f32 v[150:151], v[4:5], v[150:151] op_sel_hi:[0,1]
	v_pk_mul_f32 v[166:167], v[4:5], v[166:167] op_sel_hi:[0,1]
	s_waitcnt vmcnt(11)
	v_pk_mul_f32 v[150:151], v[212:213], v[150:151]
	v_pk_mul_f32 v[154:155], v[210:211], v[164:165]
	s_waitcnt vmcnt(10)
	v_pk_mul_f32 v[156:157], v[214:215], v[166:167]
	v_med3_f32 v147, v154, s27, v146
	v_med3_f32 v154, v155, s27, v146
	v_med3_f32 v155, v156, s27, v146
	v_med3_f32 v156, v157, s27, v146
	v_lshlrev_b32_e32 v152, 16, v201
	v_and_b32_e32 v153, 0xffff0000, v201
	v_cvt_pk_fp8_f32 v162, v147, v154
	v_cvt_pk_fp8_f32 v163, v155, v156
	v_pk_mul_f32 v[152:153], v[4:5], v[152:153] op_sel_hi:[0,1]
	v_pk_mul_f32 v[152:153], v[216:217], v[152:153]
	v_med3_f32 v150, v150, s27, v146
	v_med3_f32 v151, v151, s27, v146
	v_med3_f32 v152, v152, s27, v146
	v_med3_f32 v153, v153, s27, v146
	v_cvt_pk_fp8_f32 v162, v150, v151 op_sel:[0,0,1]
	v_cvt_pk_fp8_f32 v163, v152, v153 op_sel:[0,0,1]
	global_store_dwordx2 v[114:115], v[162:163], off offset:512
	global_store_dwordx2 v[116:117], v[162:163], off offset:512
	global_store_dwordx2 v[118:119], v[162:163], off offset:512
	global_store_dwordx2 v[120:121], v[162:163], off offset:512
	v_mov_b32_e32 v162, 0
	v_mov_b32_e32 v163, 0
	s_waitcnt vmcnt(13)
	v_lshlrev_b32_e32 v164, 16, v202
	v_and_b32_e32 v165, 0xffff0000, v202
	v_lshlrev_b32_e32 v150, 16, v203
	v_and_b32_e32 v151, 0xffff0000, v203
	v_lshlrev_b32_e32 v166, 16, v204
	v_and_b32_e32 v167, 0xffff0000, v204
	v_pk_mul_f32 v[164:165], v[4:5], v[164:165] op_sel_hi:[0,1]
	v_pk_mul_f32 v[150:151], v[4:5], v[150:151] op_sel_hi:[0,1]
	v_pk_mul_f32 v[166:167], v[4:5], v[166:167] op_sel_hi:[0,1]
	s_waitcnt vmcnt(12)
	v_pk_mul_f32 v[150:151], v[220:221], v[150:151]
	v_pk_mul_f32 v[154:155], v[218:219], v[164:165]
	s_waitcnt vmcnt(11)
	v_pk_mul_f32 v[156:157], v[222:223], v[166:167]
	v_med3_f32 v147, v154, s27, v146
	v_med3_f32 v154, v155, s27, v146
	v_med3_f32 v155, v156, s27, v146
	v_med3_f32 v156, v157, s27, v146
	v_lshlrev_b32_e32 v152, 16, v205
	v_and_b32_e32 v153, 0xffff0000, v205
	v_cvt_pk_fp8_f32 v162, v147, v154
	v_cvt_pk_fp8_f32 v163, v155, v156
	v_pk_mul_f32 v[152:153], v[4:5], v[152:153] op_sel_hi:[0,1]
	v_pk_mul_f32 v[152:153], v[224:225], v[152:153]
	v_med3_f32 v150, v150, s27, v146
	v_med3_f32 v151, v151, s27, v146
	v_med3_f32 v152, v152, s27, v146
	v_med3_f32 v153, v153, s27, v146
	v_cvt_pk_fp8_f32 v162, v150, v151 op_sel:[0,0,1]
	v_cvt_pk_fp8_f32 v163, v152, v153 op_sel:[0,0,1]
	global_store_dwordx2 v[114:115], v[162:163], off offset:1024
	global_store_dwordx2 v[116:117], v[162:163], off offset:1024
	global_store_dwordx2 v[118:119], v[162:163], off offset:1024
	global_store_dwordx2 v[120:121], v[162:163], off offset:1024
	v_mov_b32_e32 v162, 0
	v_mov_b32_e32 v163, 0
	v_lshl_add_u64 v[112:113], v[112:113], 0, s[12:13]
	s_waitcnt vmcnt(14)
	v_lshlrev_b32_e32 v164, 16, v206
	v_and_b32_e32 v165, 0xffff0000, v206
	v_lshlrev_b32_e32 v150, 16, v207
	v_and_b32_e32 v151, 0xffff0000, v207
	v_lshlrev_b32_e32 v166, 16, v208
	v_and_b32_e32 v167, 0xffff0000, v208
	v_pk_mul_f32 v[164:165], v[4:5], v[164:165] op_sel_hi:[0,1]
	v_pk_mul_f32 v[150:151], v[4:5], v[150:151] op_sel_hi:[0,1]
	v_pk_mul_f32 v[166:167], v[4:5], v[166:167] op_sel_hi:[0,1]
	v_lshlrev_b32_e32 v152, 16, v209
	v_and_b32_e32 v153, 0xffff0000, v209
	s_waitcnt vmcnt(13)
	v_pk_mul_f32 v[150:151], v[228:229], v[150:151]
	v_pk_mul_f32 v[154:155], v[226:227], v[164:165]
	s_waitcnt vmcnt(12)
	v_pk_mul_f32 v[156:157], v[230:231], v[166:167]
	v_pk_mul_f32 v[152:153], v[4:5], v[152:153] op_sel_hi:[0,1]
	v_med3_f32 v4, v154, s27, v146
	v_med3_f32 v147, v155, s27, v146
	v_med3_f32 v154, v156, s27, v146
	v_med3_f32 v155, v157, s27, v146
	v_cvt_pk_fp8_f32 v162, v4, v147
	v_cvt_pk_fp8_f32 v163, v154, v155
	v_pk_mul_f32 v[152:153], v[232:233], v[152:153]
	v_med3_f32 v150, v150, s27, v146
	v_med3_f32 v151, v151, s27, v146
	v_med3_f32 v152, v152, s27, v146
	v_med3_f32 v153, v153, s27, v146
	v_cvt_pk_fp8_f32 v162, v150, v151 op_sel:[0,0,1]
	v_cvt_pk_fp8_f32 v163, v152, v153 op_sel:[0,0,1]
	global_store_dwordx2 v[114:115], v[162:163], off offset:1536
	global_store_dwordx2 v[116:117], v[162:163], off offset:1536
	global_store_dwordx2 v[118:119], v[162:163], off offset:1536
	global_store_dwordx2 v[120:121], v[162:163], off offset:1536
	s_cbranch_scc0 .LBB0_2468
	s_branch .LBB0_2138
